# speedup vs baseline: 1.0165x; 1.0165x over previous
_Z5k0_lnPKfS0_S0_S0_PDF16_S1_S1_S0_S0_S0_S0_S0_S0_S0_S1_:
	s_cmpk_lt_u32 s2, 0x400
	s_mov_b64 s[4:5], -1
	s_cbranch_scc0 .LBB0_4
	s_load_dwordx8 s[4:11], s[0:1], 0x0
	s_lshr_b32 s18, s2, 8
	s_lshl_b32 s3, s2, 6
	s_mov_b32 s19, 0
	s_and_b32 s20, s3, 0x3fc0
	s_lshl_b64 s[22:23], s[18:19], 22
	s_waitcnt lgkmcnt(0)
	s_add_u32 s3, s4, s22
	s_addc_u32 s5, s5, s23
	s_lshl_b32 s24, s20, 2
	s_add_u32 s4, s3, s24
	v_lshlrev_b32_e32 v2, 4, v0
	s_addc_u32 s5, s5, 0
	v_lshlrev_b32_e32 v1, 10, v0
	v_and_b32_e32 v30, 0xf0, v2
	v_mov_b32_e32 v31, 0
	v_lshlrev_b32_e32 v4, 12, v0
	s_mov_b32 s3, 0x7c000
	v_mov_b32_e32 v8, 0x40000
	v_lshl_add_u64 v[2:3], s[4:5], 0, v[30:31]
	v_and_b32_e32 v4, 0xf0000, v4
	v_mov_b32_e32 v5, v31
	v_bitop3_b32 v8, v1, s3, v8 bitop3:0xc8
	v_lshl_add_u64 v[6:7], v[2:3], 0, v[4:5]
	v_lshlrev_b32_e32 v8, 2, v8
	v_mov_b32_e32 v9, v31
	v_lshl_add_u64 v[10:11], v[2:3], 0, v[8:9]
	global_load_dwordx4 v[20:23], v[6:7], off nt
	global_load_dwordx4 v[24:27], v[10:11], off nt
	s_mov_b32 s3, 0xbc000
	v_mov_b32_e32 v6, 0x80000
	v_bitop3_b32 v6, v1, s3, v6 bitop3:0xc8
	v_lshlrev_b32_e32 v6, 2, v6
	v_mov_b32_e32 v7, v31
	v_lshl_add_u64 v[10:11], v[2:3], 0, v[6:7]
	global_load_dwordx4 v[32:35], v[10:11], off nt
	s_mov_b32 s3, 0xfc000
	v_mov_b32_e32 v10, 0xc0000
	v_bitop3_b32 v1, v1, s3, v10 bitop3:0xc8
	v_lshlrev_b32_e32 v10, 2, v1
	v_mov_b32_e32 v11, v31
	v_lshl_add_u64 v[2:3], v[2:3], 0, v[10:11]
	global_load_dwordx4 v[36:39], v[2:3], off nt
	s_add_u32 s4, s6, s22
	s_addc_u32 s5, s7, s23
	v_or_b32_e32 v3, 0x200, v0
	s_add_u32 s4, s4, s24
	v_lshrrev_b32_e32 v2, 4, v0
	s_movk_i32 s3, 0x104
	v_lshrrev_b32_e32 v3, 4, v3
	s_addc_u32 s5, s5, 0
	v_or_b32_e32 v18, 0x100, v0
	v_or_b32_e32 v12, 0x300, v0
	v_and_b32_e32 v13, 63, v0
	v_lshrrev_b32_e32 v45, 2, v0
	v_mul_u32_u24_e32 v1, 0x104, v2
	v_mad_u32_u24 v51, v2, s3, v30
	v_mul_u32_u24_e32 v43, 0x104, v3
	v_mad_u32_u24 v53, v3, s3, v30
	v_lshl_add_u64 v[2:3], s[4:5], 0, v[30:31]
	v_lshrrev_b32_e32 v14, 4, v18
	v_lshrrev_b32_e32 v50, 4, v12
	v_and_b32_e32 v12, 48, v45
	v_lshlrev_b32_e32 v19, 2, v13
	v_lshl_add_u64 v[68:69], v[2:3], 0, v[4:5]
	s_load_dwordx4 s[12:15], s[0:1], 0x20
	s_load_dwordx2 s[16:17], s[0:1], 0x30
	v_mul_u32_u24_e32 v44, 0x104, v14
	v_mad_u32_u24 v52, v14, s3, v30
	v_mad_u32_u24 v55, v12, s3, v19
	v_lshl_add_u64 v[40:41], v[2:3], 0, v[8:9]
	v_lshl_add_u64 v[46:47], v[2:3], 0, v[6:7]
	v_lshl_add_u64 v[48:49], v[2:3], 0, v[10:11]
	v_mad_u32_u24 v54, v50, s3, v30
	v_add_u32_e32 v56, 0x400, v55
	v_add_u32_e32 v28, 0x800, v55
	v_lshlrev_b32_e32 v42, 2, v0
	s_mov_b32 s21, s19
	v_cmp_gt_u32_e32 vcc, 64, v0
	s_waitcnt vmcnt(3)
	ds_write2_b32 v51, v20, v21 offset1:1
	ds_write2_b32 v51, v22, v23 offset0:2 offset1:3
	s_waitcnt vmcnt(2)
	ds_write2_b32 v52, v24, v25 offset1:1
	ds_write2_b32 v52, v26, v27 offset0:2 offset1:3
	s_waitcnt vmcnt(1)
	ds_write2_b32 v53, v32, v33 offset1:1
	ds_write2_b32 v53, v34, v35 offset0:2 offset1:3
	s_waitcnt vmcnt(0)
	ds_write2_b32 v54, v36, v37 offset1:1
	ds_write2_b32 v54, v38, v39 offset0:2 offset1:3
	s_waitcnt lgkmcnt(0)
	s_barrier
	global_load_dwordx4 v[14:17], v[68:69], off nt
	global_load_dwordx4 v[10:13], v[40:41], off nt
	global_load_dwordx4 v[6:9], v[46:47], off nt
	global_load_dwordx4 v[2:5], v[48:49], off nt
	ds_read2_b32 v[20:21], v55 offset1:65
	ds_read2_b32 v[22:23], v55 offset0:130 offset1:195
	ds_read2_b32 v[24:25], v56 offset0:4 offset1:69
	ds_read2_b32 v[26:27], v56 offset0:134 offset1:199
	s_waitcnt lgkmcnt(3)
	v_add_f32_e32 v20, 0, v20
	v_add_f32_e32 v20, v20, v21
	s_waitcnt lgkmcnt(2)
	v_add_f32_e32 v20, v20, v22
	v_add_f32_e32 v20, v20, v23
	s_waitcnt lgkmcnt(1)
	v_add_f32_e32 v22, v20, v24
	ds_read2_b32 v[20:21], v28 offset0:8 offset1:73
	v_add_f32_e32 v24, v22, v25
	ds_read2_b32 v[22:23], v28 offset0:138 offset1:203
	s_waitcnt lgkmcnt(2)
	v_add_f32_e32 v24, v24, v26
	v_add_f32_e32 v24, v24, v27
	s_waitcnt lgkmcnt(1)
	v_add_f32_e32 v20, v24, v20
	v_add_f32_e32 v20, v20, v21
	v_add_u32_e32 v26, 0xc00, v55
	s_waitcnt lgkmcnt(0)
	v_add_f32_e32 v22, v20, v22
	ds_read2_b32 v[20:21], v26 offset0:12 offset1:77
	v_or_b32_e32 v24, 15, v45
	v_mad_u32_u24 v27, v24, s3, v19
	ds_read_b32 v24, v55 offset:3640
	ds_read_b32 v25, v27
	v_add_f32_e32 v22, v22, v23
	s_waitcnt lgkmcnt(2)
	v_add_f32_e32 v20, v22, v20
	v_add_f32_e32 v20, v20, v21
	s_waitcnt lgkmcnt(1)
	v_add_f32_e32 v20, v20, v24
	s_waitcnt lgkmcnt(0)
	v_add_f32_e32 v20, v20, v25
	ds_write_b32 v42, v20 offset:16640
	s_waitcnt lgkmcnt(0)
	s_barrier
	ds_read2st64_b32 v[20:21], v19 offset0:65 offset1:66
	ds_read2st64_b32 v[22:23], v19 offset0:67 offset1:68
	s_waitcnt lgkmcnt(0)
	s_barrier
	ds_read2_b32 v[24:25], v55 offset1:65
	v_add_f32_e32 v20, v20, v21
	v_add_f32_e32 v20, v20, v22
	v_add_f32_e32 v20, v20, v23
	ds_read2_b32 v[22:23], v55 offset0:130 offset1:195
	s_waitcnt lgkmcnt(1)
	v_fmac_f32_e32 v25, 0xbc800000, v20
	v_fmamk_f32 v21, v20, 0xbc800000, v24
	v_mul_f32_e32 v29, v25, v25
	ds_read2_b32 v[24:25], v56 offset0:4 offset1:69
	v_fmac_f32_e32 v29, v21, v21
	s_waitcnt lgkmcnt(1)
	v_fmamk_f32 v21, v20, 0xbc800000, v22
	v_fmac_f32_e32 v29, v21, v21
	v_fmac_f32_e32 v23, 0xbc800000, v20
	v_fmac_f32_e32 v29, v23, v23
	s_waitcnt lgkmcnt(0)
	v_fmamk_f32 v21, v20, 0xbc800000, v24
	ds_read2_b32 v[22:23], v56 offset0:134 offset1:199
	v_fmac_f32_e32 v29, v21, v21
	v_fmac_f32_e32 v25, 0xbc800000, v20
	v_fmac_f32_e32 v29, v25, v25
	ds_read2_b32 v[24:25], v28 offset0:8 offset1:73
	s_waitcnt lgkmcnt(1)
	v_fmamk_f32 v21, v20, 0xbc800000, v22
	v_fmac_f32_e32 v29, v21, v21
	v_fmac_f32_e32 v23, 0xbc800000, v20
	v_fmac_f32_e32 v29, v23, v23
	s_waitcnt lgkmcnt(0)
	v_fmamk_f32 v21, v20, 0xbc800000, v24
	ds_read2_b32 v[22:23], v28 offset0:138 offset1:203
	v_fmac_f32_e32 v29, v21, v21
	v_fmac_f32_e32 v25, 0xbc800000, v20
	v_fmac_f32_e32 v29, v25, v25
	ds_read2_b32 v[24:25], v26 offset0:12 offset1:77
	s_waitcnt lgkmcnt(1)
	v_fmamk_f32 v21, v20, 0xbc800000, v22
	v_fmac_f32_e32 v29, v21, v21
	v_fmac_f32_e32 v23, 0xbc800000, v20
	v_fmac_f32_e32 v29, v23, v23
	s_waitcnt lgkmcnt(0)
	v_fmamk_f32 v21, v20, 0xbc800000, v24
	ds_read_b32 v22, v55 offset:3640
	v_fmac_f32_e32 v29, v21, v21
	ds_read_b32 v21, v27
	v_fmac_f32_e32 v25, 0xbc800000, v20
	v_fmac_f32_e32 v29, v25, v25
	s_waitcnt lgkmcnt(1)
	v_fmac_f32_e32 v22, 0xbc800000, v20
	v_fmac_f32_e32 v29, v22, v22
	s_waitcnt lgkmcnt(0)
	v_fmac_f32_e32 v21, 0xbc800000, v20
	v_mul_u32_u24_e32 v45, 0x104, v50
	v_fmac_f32_e32 v29, v21, v21
	ds_write_b32 v42, v29 offset:16640
	s_waitcnt lgkmcnt(0)
	s_barrier
	s_and_saveexec_b64 s[6:7], vcc
	s_cbranch_execz .LBB0_3
	v_or_b32_e32 v21, 0x4100, v19
	ds_read2st64_b32 v[22:23], v21 offset1:1
	ds_read2st64_b32 v[24:25], v21 offset0:2 offset1:3
	v_mov_b32_e32 v21, 0x3727c5ac
	s_mov_b32 s4, 0xf800000
	v_mul_f32_e32 v20, 0x3c800000, v20
	s_waitcnt lgkmcnt(1)
	v_add_f32_e32 v22, v22, v23
	s_waitcnt lgkmcnt(0)
	v_add_f32_e32 v22, v22, v24
	v_add_f32_e32 v22, v22, v25
	v_fmac_f32_e32 v21, 0x3c800000, v22
	v_mul_f32_e32 v22, 0x4f800000, v21
	v_cmp_gt_f32_e32 vcc, s4, v21
	s_nop 1
	v_cndmask_b32_e32 v21, v21, v22, vcc
	v_sqrt_f32_e32 v22, v21
	s_nop 0
	v_add_u32_e32 v23, -1, v22
	v_add_u32_e32 v24, 1, v22
	v_fma_f32 v25, -v23, v22, v21
	v_fma_f32 v26, -v24, v22, v21
	v_cmp_ge_f32_e64 s[4:5], 0, v25
	s_nop 1
	v_cndmask_b32_e64 v22, v22, v23, s[4:5]
	v_cmp_lt_f32_e64 s[4:5], 0, v26
	s_nop 1
	v_cndmask_b32_e64 v22, v22, v24, s[4:5]
	v_mul_f32_e32 v23, 0x37800000, v22
	v_cndmask_b32_e32 v22, v22, v23, vcc
	v_mov_b32_e32 v23, 0x260
	v_cmp_class_f32_e32 vcc, v21, v23
	s_nop 1
	v_cndmask_b32_e32 v21, v22, v21, vcc
	v_div_scale_f32 v22, s[4:5], v21, v21, 1.0
	v_rcp_f32_e32 v23, v22
	s_nop 0
	v_fma_f32 v24, -v22, v23, 1.0
	v_fmac_f32_e32 v23, v24, v23
	v_div_scale_f32 v24, vcc, 1.0, v21, 1.0
	v_mul_f32_e32 v25, v24, v23
	v_fma_f32 v26, -v22, v25, v24
	v_fmac_f32_e32 v25, v26, v23
	v_fma_f32 v22, -v22, v25, v24
	v_div_fmas_f32 v22, v22, v23, v25
	v_div_fixup_f32 v21, v22, v21, 1.0
	ds_write2st64_b32 v19, v20, v21 offset0:69 offset1:70

	.amdhsa_kernel _Z5k0_lnPKfS0_S0_S0_PDF16_S1_S1_S0_S0_S0_S0_S0_S0_S0_S1_
		.amdhsa_group_segment_fixed_size 18176
		.amdhsa_private_segment_fixed_size 0
		.amdhsa_kernarg_size 120
		.amdhsa_user_sgpr_count 2
		.amdhsa_user_sgpr_dispatch_ptr 0
		.amdhsa_user_sgpr_queue_ptr 0
		.amdhsa_user_sgpr_kernarg_segment_ptr 1
		.amdhsa_user_sgpr_dispatch_id 0
		.amdhsa_user_sgpr_kernarg_preload_length 0
		.amdhsa_user_sgpr_kernarg_preload_offset 0
		.amdhsa_user_sgpr_private_segment_size 0
		.amdhsa_uses_dynamic_stack 0
		.amdhsa_enable_private_segment 0
		.amdhsa_system_sgpr_workgroup_id_x 1
		.amdhsa_system_sgpr_workgroup_id_y 0
		.amdhsa_system_sgpr_workgroup_id_z 0
		.amdhsa_system_sgpr_workgroup_info 0
		.amdhsa_system_vgpr_workitem_id 0
		.amdhsa_next_free_vgpr 70
		.amdhsa_next_free_sgpr 25
		.amdhsa_accum_offset 72
		.amdhsa_reserve_vcc 1
		.amdhsa_float_round_mode_32 0
		.amdhsa_float_round_mode_16_64 0
		.amdhsa_float_denorm_mode_32 3
		.amdhsa_float_denorm_mode_16_64 3
		.amdhsa_dx10_clamp 1
		.amdhsa_ieee_mode 1
		.amdhsa_fp16_overflow 0
		.amdhsa_tg_split 0
		.amdhsa_exception_fp_ieee_invalid_op 0
		.amdhsa_exception_fp_denorm_src 0
		.amdhsa_exception_fp_ieee_div_zero 0
		.amdhsa_exception_fp_ieee_overflow 0
		.amdhsa_exception_fp_ieee_underflow 0
		.amdhsa_exception_fp_ieee_inexact 0
		.amdhsa_exception_int_div_zero 0
	.end_amdhsa_kernel

amdhsa.kernels:
  - .agpr_count:     0
    .args:
      - .actual_access:  read_only
        .address_space:  global
        .offset:         0
        .size:           8
        .value_kind:     global_buffer
      - .actual_access:  read_only
        .address_space:  global
        .offset:         8
        .size:           8
        .value_kind:     global_buffer
      - .actual_access:  read_only
        .address_space:  global
        .offset:         16
        .size:           8
        .value_kind:     global_buffer
      - .actual_access:  read_only
        .address_space:  global
        .offset:         24
        .size:           8
        .value_kind:     global_buffer
      - .actual_access:  write_only
        .address_space:  global
        .offset:         32
        .size:           8
        .value_kind:     global_buffer
      - .actual_access:  write_only
        .address_space:  global
        .offset:         40
        .size:           8
        .value_kind:     global_buffer
      - .actual_access:  write_only
        .address_space:  global
        .offset:         48
        .size:           8
        .value_kind:     global_buffer
      - .actual_access:  read_only
        .address_space:  global
        .offset:         56
        .size:           8
        .value_kind:     global_buffer
      - .actual_access:  read_only
        .address_space:  global
        .offset:         64
        .size:           8
        .value_kind:     global_buffer
      - .actual_access:  read_only
        .address_space:  global
        .offset:         72
        .size:           8
        .value_kind:     global_buffer
      - .actual_access:  read_only
        .address_space:  global
        .offset:         80
        .size:           8
        .value_kind:     global_buffer
      - .actual_access:  read_only
        .address_space:  global
        .offset:         88
        .size:           8
        .value_kind:     global_buffer
      - .actual_access:  read_only
        .address_space:  global
        .offset:         96
        .size:           8
        .value_kind:     global_buffer
      - .actual_access:  read_only
        .address_space:  global
        .offset:         104
        .size:           8
        .value_kind:     global_buffer
      - .actual_access:  write_only
        .address_space:  global
        .offset:         112
        .size:           8
        .value_kind:     global_buffer
    .group_segment_fixed_size: 18176
    .kernarg_segment_align: 8
    .kernarg_segment_size: 120
    .language:       OpenCL C
    .language_version:
      - 2
      - 0
    .max_flat_workgroup_size: 256
    .name:           _Z5k0_lnPKfS0_S0_S0_PDF16_S1_S1_S0_S0_S0_S0_S0_S0_S0_S1_
    .private_segment_fixed_size: 0
    .sgpr_count:     31
    .sgpr_spill_count: 0
    .symbol:         _Z5k0_lnPKfS0_S0_S0_PDF16_S1_S1_S0_S0_S0_S0_S0_S0_S0_S1_.kd
    .uniform_work_group_size: 1
    .uses_dynamic_stack: false
    .vgpr_count:     70
    .vgpr_spill_count: 0
    .wavefront_size: 64
  - .agpr_count:     0
    .args:
      - .actual_access:  read_only
        .address_space:  global
        .offset:         0
        .size:           8
        .value_kind:     global_buffer
      - .actual_access:  read_only
        .address_space:  global
        .offset:         8
        .size:           8
        .value_kind:     global_buffer
      - .actual_access:  read_only
        .address_space:  global
        .offset:         16
        .size:           8
        .value_kind:     global_buffer
      - .actual_access:  read_only
        .address_space:  global
        .offset:         24
        .size:           8
        .value_kind:     global_buffer
      - .actual_access:  read_only
        .address_space:  global
        .offset:         32
        .size:           8
        .value_kind:     global_buffer
      - .actual_access:  write_only
        .address_space:  global
        .offset:         40
        .size:           8
        .value_kind:     global_buffer
    .group_segment_fixed_size: 149200
    .kernarg_segment_align: 8
    .kernarg_segment_size: 48
    .language:       OpenCL C
    .language_version:
      - 2
      - 0
    .max_flat_workgroup_size: 1024
    .name:           _Z6k1_mfePKDF16_PKfS2_S2_S2_PDF16_
    .private_segment_fixed_size: 0
    .sgpr_count:     30
    .sgpr_spill_count: 0
    .symbol:         _Z6k1_mfePKDF16_PKfS2_S2_S2_PDF16_.kd
    .uniform_work_group_size: 1
    .uses_dynamic_stack: false
    .vgpr_count:     50
    .vgpr_spill_count: 0
    .wavefront_size: 64
  - .agpr_count:     0
    .args:
      - .actual_access:  read_only
        .address_space:  global
        .offset:         0
        .size:           8
        .value_kind:     global_buffer
      - .actual_access:  read_only
        .address_space:  global
        .offset:         8
        .size:           8
        .value_kind:     global_buffer
      - .actual_access:  read_only
        .address_space:  global
        .offset:         16
        .size:           8
        .value_kind:     global_buffer
      - .actual_access:  read_only
        .address_space:  global
        .offset:         24
        .size:           8
        .value_kind:     global_buffer
      - .actual_access:  write_only
        .address_space:  global
        .offset:         32
        .size:           8
        .value_kind:     global_buffer
      - .actual_access:  write_only
        .address_space:  global
        .offset:         40
        .size:           8
        .value_kind:     global_buffer
      - .actual_access:  write_only
        .address_space:  global
        .offset:         48
        .size:           8
        .value_kind:     global_buffer
    .group_segment_fixed_size: 71424
    .kernarg_segment_align: 8
    .kernarg_segment_size: 56
    .language:       OpenCL C
    .language_version:
      - 2
      - 0
    .max_flat_workgroup_size: 512
    .name:           _Z5k2_kvPKDF16_S0_S0_S0_PDF16_S1_Pf
    .private_segment_fixed_size: 0
    .sgpr_count:     33
    .sgpr_spill_count: 0
    .symbol:         _Z5k2_kvPKDF16_S0_S0_S0_PDF16_S1_Pf.kd
    .uniform_work_group_size: 1
    .uses_dynamic_stack: false
    .vgpr_count:     114
    .vgpr_spill_count: 0
    .wavefront_size: 64
  - .agpr_count:     0
    .args:
      - .actual_access:  read_only
        .address_space:  global
        .offset:         0
        .size:           8
        .value_kind:     global_buffer
      - .actual_access:  write_only
        .address_space:  global
        .offset:         8
        .size:           8
        .value_kind:     global_buffer
    .group_segment_fixed_size: 1024
    .kernarg_segment_align: 8
    .kernarg_segment_size: 16
    .language:       OpenCL C
    .language_version:
      - 2
      - 0
    .max_flat_workgroup_size: 256
    .name:           _Z9k3_reducePKfPf
    .private_segment_fixed_size: 0
    .sgpr_count:     13
    .sgpr_spill_count: 0
    .symbol:         _Z9k3_reducePKfPf.kd
    .uniform_work_group_size: 1
    .uses_dynamic_stack: false
    .vgpr_count:     50
    .vgpr_spill_count: 0
    .wavefront_size: 64
  - .agpr_count:     0
    .args:
      - .actual_access:  read_only
        .address_space:  global
        .offset:         0
        .size:           8
        .value_kind:     global_buffer
      - .actual_access:  read_only
        .address_space:  global
        .offset:         8
        .size:           8
        .value_kind:     global_buffer
      - .actual_access:  read_only
        .address_space:  global
        .offset:         16
        .size:           8
        .value_kind:     global_buffer
      - .actual_access:  read_only
        .address_space:  global
        .offset:         24
        .size:           8
        .value_kind:     global_buffer
      - .actual_access:  read_only
        .address_space:  global
        .offset:         32
        .size:           8
        .value_kind:     global_buffer
      - .actual_access:  read_only
        .address_space:  global
        .offset:         40
        .size:           8
        .value_kind:     global_buffer
      - .actual_access:  read_only
        .address_space:  global
        .offset:         48
        .size:           8
        .value_kind:     global_buffer
      - .actual_access:  read_only
        .address_space:  global
        .offset:         56
        .size:           8
        .value_kind:     global_buffer
      - .actual_access:  write_only
        .address_space:  global
        .offset:         64
        .size:           8
        .value_kind:     global_buffer
    .group_segment_fixed_size: 74752
    .kernarg_segment_align: 8
    .kernarg_segment_size: 72
    .language:       OpenCL C
    .language_version:
      - 2
      - 0
    .max_flat_workgroup_size: 512
    .name:           _Z8k4_fusedPKfPKDF16_S2_S0_S0_S2_S0_S0_Pf
    .private_segment_fixed_size: 0
    .sgpr_count:     108
    .sgpr_spill_count: 0
    .symbol:         _Z8k4_fusedPKfPKDF16_S2_S0_S0_S2_S0_S0_Pf.kd
    .uniform_work_group_size: 1
    .uses_dynamic_stack: false
    .vgpr_count:     128
    .vgpr_spill_count: 0
    .wavefront_size: 64
